# three-epilogue version padded (dead 60 bytes) so every hot loop starts at the same offset mod 64 as in the out-projection-only version
# speedup vs baseline: 1.0107x; 1.0107x over previous
;     __device__ __forceinline__ bool next(int i, Unit& u) const { if (!order_tile(i, G, c, nM, nN, u.pm, u.pn)) return false; u.A = A0 + (size_t)u.pm * tstep; u.B = B0 + (size_t)u.pn * tstep; return true; }
;     __device__ __forceinline__ bool next(int i, Unit& u) const { if (!order_tile(i, G, c, nM, nN, u.pm, u.pn)) return false; u.A = A0 + (size_t)(u.pn >> 1) * groupA + (size_t)u.pm * tstep; u.B = B0 + (size_t)u.pn * tstep; return true; }
; #define PG8_STAGE(bufoff, gbase, voff) do { _Pragma("unroll") for (int _i = 0; _i < 2; ++_i) glds16_s((const void*)((const char*)(gbase) + _i * r64), (voff), ldsb + (unsigned)(bufoff) + ldsw + _i * 8192u); } while (0)
; #define PG8_WAIT_V(n) asm volatile("s_waitcnt vmcnt(" #n ")" ::: "memory")
; #define PG8_BAR __builtin_amdgcn_s_barrier()
; template <class Epi, class Sched, bool FP8 = false>
; __device__ __forceinline__ void gemm_phase(LAS unsigned char* lds, const int Kb, const int nt  , const Sched& S, const Epi& E) {
;     ...
;     { int R, C; stage_rc(tid * 16, R, C); const int Rb = Epi::PERM ? ((R & ~31) + perm32(R & 31)) : R;
;         voffA = (unsigned)(R * Kb + C * 2); voffB = (unsigned)(Rb * Kb + C * 2); }
;     const size_t r64 = (size_t)64 * Kb;
;     const size_t kstep = (size_t)(BK * 2);
;     const size_t hstep = (size_t)HALF * Kb;
;     const unsigned ldsw = (unsigned)wid * 1024u, ldsb = (unsigned)(uintptr_t)lds;
;     const int aoff = lds_byte(wr * 64 + fr, fq * 8), boff = lds_byte(wc * 32 + fr, fq * 8);
;     ...
;     Unit cur, nxt; int ui = 0;
;     if (!S.next(0, cur)) return;
;     f32x4 acc[2][2][4][2];
; #pragma unroll
;     for (int a = 0; a < 2; ++a)
; #pragma unroll
;         for (int b = 0; b < 2; ++b)
; #pragma unroll
;             for (int m = 0; m < 4; ++m)
; #pragma unroll
;                 for (int n = 0; n < 2; ++n) acc[a][b][m][n] = (f32x4){0.f, 0.f, 0.f, 0.f};
;     bf16x8 At[4][2], B0[2][2], B1[2][2]; i32x8 A8[4], B08[2], B18[2];
;     const char* cA = cur.A; const char* cB = cur.B;
;     PG8_STAGE(PG8_SB(0, 0), cB, voffB); PG8_STAGE(PG8_SA(0, 0), cA, voffA); PG8_STAGE(PG8_SB(0, 1), cB + hstep, voffB); PG8_STAGE(PG8_SA(0, 1), cA + hstep, voffA);
;     if (wr == 1) PG8_BAR;
;     PG8_WAIT_V(4); PG8_BAR;
;     PG8_STAGE(PG8_SB(1, 0), cB + kstep, voffB); PG8_STAGE(PG8_SA(1, 0), cA + kstep, voffA); PG8_STAGE(PG8_SB(1, 1), cB + hstep + kstep, voffB);
;     PG8_WAIT_V(6); PG8_BAR;
.LBB0_2323:
	s_ashr_i32 s61, s4, 3
	v_readlane_b32 s6, v241, 5
	v_readlane_b32 s7, v241, 6
	s_add_u32 s4, s6, 0x5af00000
	s_addc_u32 s5, s7, 0
	s_add_u32 s6, s6, 0x56f00000
	s_addc_u32 s7, s7, 0
	s_lshl_b32 s8, s8, 5
	s_and_b32 s51, s8, 0x60
	s_lshl_b32 s50, s9, 6
	s_lshl_b32 s10, s9, 13
	s_lshl_b32 s11, s51, 7
	s_add_u32 s8, s28, 0x80
	s_addc_u32 s9, s29, 0
	s_add_i32 s52, s42, 0x18000
	s_waitcnt vmcnt(4)
	s_barrier
	s_mov_b32 s12, m0
	s_mov_b32 m0, s52
	s_nop 0
	global_load_lds_dwordx4 v1, s[8:9]
	s_mov_b32 m0, s12
	s_add_u32 s8, s28, 0x10080
	s_addc_u32 s9, s29, 0
	s_add_i32 s53, s42, 0x1a000
	s_mov_b32 s12, m0
	s_mov_b32 m0, s53
	s_nop 0
	global_load_lds_dwordx4 v1, s[8:9]
	s_mov_b32 m0, s12
	s_add_u32 s8, s0, 0x80
	s_addc_u32 s9, s1, 0
	s_add_i32 s54, s42, 0x8000
	s_mov_b32 s12, m0
	s_mov_b32 m0, s54
	s_nop 0
	global_load_lds_dwordx4 v1, s[8:9]
	s_mov_b32 m0, s12
	s_add_u32 s8, s0, 0x10080
	s_addc_u32 s9, s1, 0
	s_add_i32 s55, s42, 0xa000
	s_mov_b32 s12, m0
	s_mov_b32 m0, s55
	s_nop 0
	global_load_lds_dwordx4 v1, s[8:9]
	s_mov_b32 m0, s12
	s_add_u32 s8, s28, 0x20080
	s_addc_u32 s9, s29, 0
	s_add_i32 s56, s42, 0x1c000
	v_lshlrev_b32_e32 v3, 6, v0
	v_lshlrev_b32_e32 v4, 2, v0
	s_mov_b32 s12, m0
	s_mov_b32 m0, s56
	s_nop 0
	global_load_lds_dwordx4 v1, s[8:9]
	s_mov_b32 m0, s12
	s_add_u32 s8, s28, 0x30080
	v_and_b32_e32 v2, 48, v0
	v_and_b32_e32 v3, 0x3c0, v3
	v_and_b32_e32 v4, 32, v4
	s_addc_u32 s9, s29, 0
	s_add_i32 s57, s42, 0x1e000
	s_mov_b32 s12, m0
	s_mov_b32 m0, s57
	s_nop 0
	global_load_lds_dwordx4 v1, s[8:9]
	s_mov_b32 m0, s12
	v_readlane_b32 s80, v241, 26
	v_bitop3_b32 v2, v3, v4, v2 bitop3:0x36
	s_waitcnt vmcnt(6)
	s_add_i32 s8, s11, 0
	s_add_i32 s58, s42, 0xc000
	s_add_i32 s59, s42, 0xe000
	v_readlane_b32 s94, v241, 40
	v_readlane_b32 s95, v241, 41
	v_add_u32_e32 v3, s8, v2
	v_add_u32_e32 v2, 0, v2
	s_cmp_lg_u64 s[94:95], 0
	s_waitcnt vmcnt(0)
	v_add_u32_e32 v150, 0x10000, v3
	v_add_u32_e32 v151, 0x10400, v3
	v_add_u32_e32 v152, 0x10800, v3
	v_add_u32_e32 v153, 0x10c00, v3
	v_add_u32_e32 v154, 0x14000, v3
	v_add_u32_e32 v155, 0x14400, v3
	v_add_u32_e32 v156, 0x14800, v3
	v_add_u32_e32 v157, 0x14c00, v3
	v_add_u32_e32 v158, 0x18000, v3
	v_add_u32_e32 v159, 0x18400, v3
	v_add_u32_e32 v160, 0x18800, v3
	v_add_u32_e32 v161, 0x18c00, v3
	v_add_u32_e32 v162, 0x1c000, v3
	v_add_u32_e32 v163, 0x1c400, v3
	v_add_u32_e32 v164, 0x1c800, v3
	v_add_u32_e32 v165, 0x1cc00, v3
	s_cselect_b64 s[8:9], -1, 0
	v_add_u32_e32 v166, s10, v2
	s_mov_b64 s[10:11], 0x100000
	s_mov_b64 s[12:13], 0x120000
	s_mov_b64 s[14:15], 0x140000
	s_mov_b64 s[16:17], 0x160000
	s_mov_b64 s[22:23], s[0:1]
	s_mov_b64 s[24:25], s[28:29]
	s_barrier
	v_readlane_b32 s81, v241, 27
	v_readlane_b32 s82, v241, 28
	v_readlane_b32 s83, v241, 29
	v_readlane_b32 s84, v241, 30
	v_readlane_b32 s85, v241, 31
	v_readlane_b32 s86, v241, 32
	v_readlane_b32 s87, v241, 33
	v_readlane_b32 s88, v241, 34
	v_readlane_b32 s89, v241, 35
	v_readlane_b32 s90, v241, 36
	v_readlane_b32 s91, v241, 37
	v_readlane_b32 s92, v241, 38
	v_readlane_b32 s93, v241, 39
	s_branch .LBB0_2325
	s_nop 0
	s_nop 0
	s_nop 0
	s_nop 0
	s_nop 0
	s_nop 0
	s_nop 0
	s_nop 0
	s_nop 0
	s_nop 0
	s_nop 0
	s_nop 0
	s_nop 0
	s_nop 0
	s_nop 0
